# v85 + ATT1 compressed branch: importance-table updates via permlane32_swap + single store instead of 8 LDS read-modify-write round trips per tile
# baseline (speedup 1.0000x reference)
.LBB0_1658:
	s_mul_i32 s0, s7, 0x4400
	v_add_u32_e32 v101, s0, v89
	s_add_i32 s8, s6, 1
	v_add3_u32 v32, v101, v92, v93
	s_cmp_lt_u32 s6, s69
	s_waitcnt vmcnt(0)
	ds_write_b128 v32, v[68:71]
	v_lshl_add_u32 v32, v88, 11, v101
	s_cselect_b32 s64, s8, s6
	v_add3_u32 v32, v32, v94, v90
	s_lshl_b64 s[0:1], s[64:65], 12
	ds_write_b128 v32, v[64:67] offset:4608
	v_lshl_add_u64 v[32:33], v[76:77], 0, s[0:1]
	v_lshl_add_u64 v[34:35], v[80:81], 0, s[0:1]
	global_load_dwordx4 v[68:71], v[32:33], off
	global_load_dwordx4 v[64:67], v[34:35], off
	v_add3_u32 v106, v101, v95, v91
	s_waitcnt lgkmcnt(0)
	s_barrier
	ds_read_b128 v[32:35], v106
	ds_read_b128 v[102:105], v106 offset:32
	s_waitcnt lgkmcnt(1)
	v_mfma_f32_32x32x16_bf16 v[32:47], v[32:35], v[60:63], 0
	v_cmp_gt_u32_e32 vcc, s67, v82
	v_cmp_le_i32_e64 s[0:1], v82, v78
	s_and_b64 vcc, vcc, s[0:1]
	v_cmp_lt_i32_e64 s[0:1], v82, v78
	s_waitcnt lgkmcnt(0)
	v_mfma_f32_32x32x16_bf16 v[32:47], v[102:105], v[48:51], v[32:47]
	ds_read_b128 v[102:105], v106 offset:64
	s_waitcnt lgkmcnt(0)
	v_mfma_f32_32x32x16_bf16 v[32:47], v[102:105], v[52:55], v[32:47]
	ds_read_b128 v[102:105], v106 offset:96
	v_or_b32_e32 v106, 2, v82
	v_cmp_le_i32_e64 s[2:3], v106, v78
	s_waitcnt lgkmcnt(0)
	v_mfma_f32_32x32x16_bf16 v[32:47], v[102:105], v[56:59], v[32:47]
	v_add_u32_e32 v102, 1, v82
	v_or_b32_e32 v103, 3, v82
	v_cmp_le_i32_e64 s[4:5], v103, v73
	s_nop 8
	v_fma_f32 v32, v32, s66, -v97
	v_exp_f32_e32 v32, v32
	v_fma_f32 v33, v33, s66, -v97
	v_exp_f32_e32 v33, v33
	v_mul_f32_e32 v32, v84, v32
	v_cndmask_b32_e32 v32, 0, v32, vcc
	v_cmp_gt_u32_e32 vcc, s67, v102
	v_mul_f32_e32 v33, v84, v33
	s_and_b64 vcc, vcc, s[0:1]
	v_cndmask_b32_e32 v102, 0, v33, vcc
	v_fma_f32 v33, v34, s66, -v97
	v_exp_f32_e32 v34, v33
	v_fma_f32 v33, v35, s66, -v97
	v_exp_f32_e32 v35, v33
	v_cmp_gt_u32_e64 s[0:1], s67, v103
	s_and_b64 s[0:1], s[0:1], s[4:5]
	s_mov_b32 s98, 0
	s_mov_b32 s99, -1
	v_add_u32_e32 v103, v98, v82
	v_pk_mul_f32 v[104:105], v[84:85], v[34:35]
	v_cmp_gt_u32_e32 vcc, s67, v106
	v_cndmask_b32_e64 v34, 0, v105, s[0:1]
	ds_read_b32 v105, v103
	s_and_b64 vcc, vcc, s[2:3]
	v_cndmask_b32_e32 v35, 0, v104, vcc
	v_add_f32_e32 v104, v102, v32
	v_add_f32_e32 v104, v35, v104
	v_fmac_f32_e32 v104, 0.5, v34
	v_mul_f32_e32 v106, 0.5, v34
	v_mov_b32_e32 v107, v106
	s_nop 1
	v_permlane32_swap_b32 v106, v107
	v_cndmask_b32_e64 v106, 0, v106, s[98:99]
	v_add_f32_e32 v104, v104, v106
	s_waitcnt lgkmcnt(0)
	v_add_f32_e32 v104, v105, v104
	ds_write_b32 v103, v104
	v_mov_b32_e32 v33, v82
	v_fma_f32 v36, v36, s66, -v97
	v_fma_f32 v37, v37, s66, -v97
	v_exp_f32_e32 v36, v36
	v_exp_f32_e32 v37, v37
	v_fma_f32 v38, v38, s66, -v97
	v_fma_f32 v39, v39, s66, -v97
	v_or_b32_e32 v107, 8, v82
	v_exp_f32_e32 v38, v38
	v_exp_f32_e32 v39, v39
	v_or_b32_e32 v106, 9, v33
	v_cmp_gt_u32_e32 vcc, s67, v107
	v_cmp_le_i32_e64 s[2:3], v107, v78
	v_cmp_gt_u32_e64 s[0:1], s67, v106
	v_pk_mul_f32 v[104:105], v[84:85], v[36:37]
	v_cmp_le_i32_e64 s[4:5], v106, v73
	s_and_b64 vcc, vcc, s[2:3]
	v_or_b32_e32 v107, 10, v82
	s_and_b64 s[0:1], s[0:1], s[4:5]
	v_cndmask_b32_e32 v37, 0, v104, vcc
	v_cmp_gt_u32_e32 vcc, s67, v107
	v_cmp_le_i32_e64 s[2:3], v107, v78
	v_cndmask_b32_e64 v36, 0, v105, s[0:1]
	v_pk_mul_f32 v[104:105], v[84:85], v[38:39]
	s_and_b64 vcc, vcc, s[2:3]
	v_or_b32_e32 v106, 11, v33
	v_cndmask_b32_e32 v39, 0, v104, vcc
	v_cmp_gt_u32_e64 s[0:1], s67, v106
	v_cmp_le_i32_e64 s[4:5], v106, v73
	s_and_b64 s[0:1], s[0:1], s[4:5]
	v_add_f32_e32 v106, v37, v36
	v_cndmask_b32_e64 v38, 0, v105, s[0:1]
	v_add_f32_e32 v106, v39, v106
	v_fmac_f32_e32 v106, 0.5, v38
	v_mul_f32_e32 v104, 0.5, v34
	v_mul_f32_e32 v105, 0.5, v38
	s_nop 1
	v_permlane32_swap_b32 v104, v105
	v_cndmask_b32_e64 v104, v105, v104, s[98:99]
	v_add_f32_e32 v104, v106, v104
	ds_write_b32 v103, v104 offset:8
	v_fma_f32 v40, v40, s66, -v97
	v_fma_f32 v41, v41, s66, -v97
	v_exp_f32_e32 v40, v40
	v_exp_f32_e32 v41, v41
	v_fma_f32 v42, v42, s66, -v97
	v_fma_f32 v43, v43, s66, -v97
	v_or_b32_e32 v107, 16, v82
	v_exp_f32_e32 v42, v42
	v_exp_f32_e32 v43, v43
	v_or_b32_e32 v106, 17, v33
	v_cmp_gt_u32_e32 vcc, s67, v107
	v_cmp_le_i32_e64 s[2:3], v107, v78
	v_cmp_gt_u32_e64 s[0:1], s67, v106
	v_pk_mul_f32 v[104:105], v[84:85], v[40:41]
	v_cmp_le_i32_e64 s[4:5], v106, v73
	s_and_b64 vcc, vcc, s[2:3]
	v_or_b32_e32 v107, 18, v82
	s_and_b64 s[0:1], s[0:1], s[4:5]
	v_cndmask_b32_e32 v41, 0, v104, vcc
	v_cmp_gt_u32_e32 vcc, s67, v107
	v_cmp_le_i32_e64 s[2:3], v107, v78
	v_cndmask_b32_e64 v40, 0, v105, s[0:1]
	v_pk_mul_f32 v[104:105], v[84:85], v[42:43]
	s_and_b64 vcc, vcc, s[2:3]
	v_or_b32_e32 v106, 19, v33
	v_cndmask_b32_e32 v43, 0, v104, vcc
	v_cmp_gt_u32_e64 s[0:1], s67, v106
	v_cmp_le_i32_e64 s[4:5], v106, v73
	s_and_b64 s[0:1], s[0:1], s[4:5]
	v_add_f32_e32 v106, v41, v40
	v_cndmask_b32_e64 v42, 0, v105, s[0:1]
	v_add_f32_e32 v106, v43, v106
	v_fmac_f32_e32 v106, 0.5, v42
	v_mul_f32_e32 v104, 0.5, v38
	v_mul_f32_e32 v105, 0.5, v42
	s_nop 1
	v_permlane32_swap_b32 v104, v105
	v_cndmask_b32_e64 v104, v105, v104, s[98:99]
	v_add_f32_e32 v104, v106, v104
	ds_write_b32 v103, v104 offset:16
	v_fma_f32 v44, v44, s66, -v97
	v_fma_f32 v45, v45, s66, -v97
	v_exp_f32_e32 v44, v44
	v_exp_f32_e32 v45, v45
	v_fma_f32 v46, v46, s66, -v97
	v_fma_f32 v47, v47, s66, -v97
	v_or_b32_e32 v106, 25, v33
	v_exp_f32_e32 v46, v46
	v_exp_f32_e32 v47, v47
	v_or_b32_e32 v107, 24, v82
	v_cmp_gt_u32_e64 s[0:1], s67, v106
	v_cmp_le_i32_e64 s[4:5], v106, v73
	v_cmp_gt_u32_e32 vcc, s67, v107
	v_pk_mul_f32 v[104:105], v[84:85], v[44:45]
	v_cmp_le_i32_e64 s[2:3], v107, v78
	s_and_b64 s[0:1], s[0:1], s[4:5]
	v_or_b32_e32 v33, 27, v33
	v_cndmask_b32_e64 v44, 0, v105, s[0:1]
	s_and_b64 vcc, vcc, s[2:3]
	v_cmp_gt_u32_e64 s[0:1], s67, v33
	v_cmp_le_i32_e64 s[4:5], v33, v73
	v_cndmask_b32_e32 v45, 0, v104, vcc
	v_or_b32_e32 v104, 26, v82
	v_pk_mul_f32 v[46:47], v[84:85], v[46:47]
	s_and_b64 s[0:1], s[0:1], s[4:5]
	v_cmp_gt_u32_e32 vcc, s67, v104
	v_cmp_le_i32_e64 s[2:3], v104, v78
	v_cndmask_b32_e64 v33, 0, v47, s[0:1]
	s_and_b64 vcc, vcc, s[2:3]
	v_cndmask_b32_e32 v46, 0, v46, vcc
	v_add_f32_e32 v105, v45, v44
	v_add_f32_e32 v105, v46, v105
	v_fmac_f32_e32 v105, 0.5, v33
	v_mul_f32_e32 v47, 0.5, v42
	v_mul_f32_e32 v104, 0.5, v33
	s_nop 1
	v_permlane32_swap_b32 v47, v104
	v_cndmask_b32_e64 v47, v104, v47, s[98:99]
	v_add_f32_e32 v47, v105, v47
	ds_write_b32 v103, v47 offset:24
	v_add_u32_e32 v104, 6, v87
	v_cmp_gt_u32_e32 vcc, 63, v104
	s_and_b64 vcc, vcc, s[98:99]
	s_and_saveexec_b64 s[0:1], vcc
	v_mul_f32_e32 v104, 0.5, v33
	ds_write_b32 v103, v104 offset:28
	s_branch .LBB0_1657
